# prio + PREP1 remap + NA bias fix + L0 attention idle workgroups convert 6 instead of 9 tiles per wave
# baseline (speedup 1.0000x reference)
.LBB0_643:
	s_not_b32 s0, s41
	s_add_i32 s42, s46, s0
	s_mov_b64 s[0:1], -1
	s_cmpk_gt_i32 s42, 0x87
	s_waitcnt vmcnt(0)
	v_lshlrev_b32_e32 v172, 2, v184
	s_cbranch_scc0 .LBB0_720
	s_ashr_i32 s0, s47, 6
	s_lshl_b32 s1, s41, 3
	s_add_i32 s40, s1, s0
	s_add_u32 s41, s6, 0x17458000
	s_mulk_i32 s0, 0x2400
	s_addc_u32 s43, s7, 0
	s_add_i32 s0, s0, 0
	s_add_u32 s44, s6, 0x7458000
	s_addc_u32 s45, s7, 0
	s_add_u32 s47, s6, 0x6458000
	s_addc_u32 s48, s7, 0
	s_add_u32 s49, s6, 0x5458000
	s_addc_u32 s50, s7, 0
	s_add_u32 s51, s6, 0x4d58000
	s_addc_u32 s52, s7, 0
	s_add_u32 s53, s6, 0x158000
	s_addc_u32 s54, s7, 0
	s_add_u32 s55, s6, 0x3390c000
	v_lshlrev_b32_e32 v2, 4, v184
	s_addc_u32 s56, s7, 0
	v_lshlrev_b32_e32 v0, 2, v184
	v_and_b32_e32 v78, 48, v2
	s_add_u32 s57, s6, 0x35e0c000
	v_lshlrev_b32_e32 v2, 1, v184
	v_and_b32_e32 v82, 48, v184
	v_and_b32_e32 v0, 60, v0
	v_bfe_u32 v83, v184, 2, 4
	s_addc_u32 s58, s7, 0
	v_and_b32_e32 v2, 0x60, v2
	v_and_b32_e32 v8, 7, v184
	v_bfe_u32 v87, v184, 3, 3
	v_mov_b32_e32 v77, 0
	v_add_u32_e32 v1, s0, v82
	v_mul_u32_u24_e32 v3, 0x50, v0
	v_add_u32_e32 v4, s0, v78
	v_mul_u32_u24_e32 v5, 0x50, v83
	s_add_u32 s59, s6, 0x3760c000
	v_add_u32_e32 v6, s0, v2
	v_mul_u32_u24_e32 v7, 0x90, v0
	v_lshlrev_b32_e32 v2, 3, v8
	v_lshl_add_u32 v8, v8, 4, s0
	v_mul_u32_u24_e32 v9, 0x90, v87
	s_mul_i32 s40, s40, 6
	s_mov_b32 s1, 0
	v_mov_b32_e32 v79, v77
	v_or_b32_e32 v84, 16, v83
	v_or_b32_e32 v85, 32, v83
	v_or_b32_e32 v86, 48, v83
	s_addc_u32 s60, s7, 0
	v_or_b32_e32 v88, 8, v87
	v_or_b32_e32 v89, 16, v87
	v_or_b32_e32 v90, 24, v87
	v_or_b32_e32 v91, 32, v87
	v_or_b32_e32 v92, 40, v87
	v_or_b32_e32 v93, 48, v87
	v_or_b32_e32 v94, 56, v87
	s_mov_b32 s65, -6
	s_addk_i32 s40, -3
	s_add_i32 s61, 0, 0x204f8
	s_movk_i32 s62, 0x2000
	s_movk_i32 s63, 0x4000
	s_movk_i32 s64, 0x6000
	s_mov_b32 s66, 0x12000
	s_mov_b32 s67, 0xc3e00000
	v_add_u32_e32 v95, v1, v3
	v_add_u32_e32 v96, v4, v5
	s_movk_i32 s68, 0x3000
	s_movk_i32 s69, 0x5000
	s_movk_i32 s70, 0x7000
	s_add_i32 s71, 0, 0x204c0
	s_add_i32 s72, 0, 0x204b8
	s_add_i32 s73, 0, 0x204b0
	s_add_i32 s74, 0, 0x204a8
	s_add_i32 s75, 0, 0x20458
	s_add_i32 s76, 0, 0x20448
	s_add_i32 s77, 0, 0x20440
	s_mov_b32 s78, 0x9000
	s_mov_b32 s79, 0x1b000
	s_mov_b32 s80, 0x25000
	s_mov_b32 s81, 0x2e000
	s_mov_b32 s82, 0x37000
	s_mov_b32 s83, 0x41000
	s_mov_b32 s84, 0x4a000
	s_mov_b32 s85, 0x53000
	s_mov_b32 s86, 0x5d000
	s_mov_b32 s87, 0x66000
	s_mov_b32 s88, 0x6f000
	s_mov_b32 s89, 0x79000
	s_mov_b32 s90, 0x82000
	s_mov_b32 s91, 0x8b000
	v_add_u32_e32 v97, v6, v7
	v_lshlrev_b32_e32 v76, 1, v2
	v_lshlrev_b32_e32 v80, 2, v0
	v_mov_b32_e32 v98, 0x43e00000
	v_mov_b32_e32 v100, v77
	v_mov_b32_e32 v101, v77
	v_mov_b32_e32 v102, v77
	v_mov_b32_e32 v103, v77
	v_add_u32_e32 v99, v8, v9
	s_branch .LBB0_647

.LBB0_1058:
	s_add_i32 s1, s40, 0xffffff78
	s_lshl_b32 s0, s38, 3
	s_max_i32 s1, s1, 0
	s_mulk_i32 s1, 48
	s_add_i32 s0, s42, s0
	s_add_i32 s43, s0, s1
	s_cmpk_gt_i32 s43, 0x5fff
	s_mov_b32 s1, 0
	s_cbranch_scc1 .LBB0_1135
	s_lshl_b32 s44, s40, 3
	s_add_u32 s45, s10, 0x17458000
	s_mul_i32 s0, s42, 0x2400
	s_addc_u32 s46, s11, 0
	s_add_i32 s0, s0, 0
	s_add_u32 s47, s10, 0x7458000
	s_addc_u32 s48, s11, 0
	s_add_u32 s49, s10, 0x6458000
	s_addc_u32 s50, s11, 0
	s_add_u32 s51, s10, 0x5458000
	s_addc_u32 s52, s11, 0
	s_add_u32 s53, s10, 0x4d58000
	s_addc_u32 s54, s11, 0
	s_add_u32 s55, s10, 0x158000
	s_addc_u32 s56, s11, 0
	s_add_u32 s57, s10, 0x3390c000
	s_addc_u32 s58, s11, 0
	s_add_u32 s59, s10, 0x35e0c000
	v_lshlrev_b32_e32 v2, 1, v86
	v_and_b32_e32 v0, 60, v0
	v_and_b32_e32 v80, 48, v54
	s_addc_u32 s60, s11, 0
	v_and_b32_e32 v2, 0x60, v2
	v_and_b32_e32 v8, 7, v85
	v_lshrrev_b32_e32 v90, 3, v86
	v_mov_b32_e32 v79, 0
	v_add_u32_e32 v1, s0, v76
	v_mul_u32_u24_e32 v3, 0x50, v0
	v_add_u32_e32 v4, s0, v80
	v_mul_u32_u24_e32 v5, 0x50, v87
	s_add_u32 s61, s10, 0x3760c000
	v_add_u32_e32 v6, s0, v2
	v_mul_u32_u24_e32 v7, 0x90, v0
	v_lshlrev_b32_e32 v2, 3, v8
	v_lshl_add_u32 v8, v8, 4, s0
	v_mul_u32_u24_e32 v9, 0x90, v90
	v_mov_b32_e32 v81, v79
	v_or_b32_e32 v77, 16, v87
	v_or_b32_e32 v88, 32, v87
	v_or_b32_e32 v89, 48, v87
	s_addc_u32 s62, s11, 0
	v_or_b32_e32 v91, 8, v90
	v_or_b32_e32 v92, 16, v90
	v_or_b32_e32 v93, 24, v90
	v_or_b32_e32 v94, 32, v90
	v_or_b32_e32 v95, 40, v90
	v_or_b32_e32 v96, 48, v90
	v_or_b32_e32 v97, 56, v90
	s_add_i32 s63, 0, 0x204f8
	s_movk_i32 s64, 0x2000
	s_movk_i32 s65, 0x4000
	s_movk_i32 s66, 0x6000
	s_mov_b32 s67, 0x12000
	s_mov_b32 s68, 0xc3e00000
	v_add_u32_e32 v98, v1, v3
	v_add_u32_e32 v99, v4, v5
	s_movk_i32 s69, 0x3000
	s_movk_i32 s70, 0x5000
	s_movk_i32 s71, 0x7000
	s_add_i32 s72, 0, 0x204c0
	s_add_i32 s73, 0, 0x204b8
	s_add_i32 s74, 0, 0x204b0
	s_add_i32 s75, 0, 0x204a8
	s_add_i32 s76, 0, 0x20458
	s_add_i32 s77, 0, 0x20448
	s_add_i32 s78, 0, 0x20440
	s_mov_b32 s79, 0x9000
	s_mov_b32 s80, 0x1b000
	s_mov_b32 s81, 0x25000
	s_mov_b32 s82, 0x2e000
	s_mov_b32 s83, 0x37000
	s_mov_b32 s84, 0x41000
	s_mov_b32 s85, 0x4a000
	s_mov_b32 s86, 0x53000
	s_mov_b32 s87, 0x5d000
	s_mov_b32 s88, 0x66000
	s_mov_b32 s89, 0x6f000
	s_mov_b32 s90, 0x79000
	s_mov_b32 s91, 0x82000
	s_mov_b32 s92, 0x8b000
	v_add_u32_e32 v100, v6, v7
	v_lshlrev_b32_e32 v78, 1, v2
	v_lshlrev_b32_e32 v82, 2, v0
	v_mov_b32_e32 v101, 0x43e00000
	v_mov_b32_e32 v104, v79
	v_mov_b32_e32 v105, v79
	v_mov_b32_e32 v106, v79
	v_mov_b32_e32 v107, v79
	v_add_u32_e32 v102, v8, v9
	s_branch .LBB0_1062
